# g11: g10 + P1 GEMM first K-loop trip peeled with inline-0 C operands instead of 128 v_mov_b32 zeroing per unit
# speedup vs baseline: 1.0155x; 1.0017x over previous
.LBB0_85:
	s_ashr_i32 s19, s18, 31
	s_lshl_b64 s[20:21], s[18:19], 20
	s_add_u32 s20, s6, s20
	s_addc_u32 s21, s7, s21
	s_and_b64 s[22:23], s[4:5], exec
	s_cselect_b32 s19, s21, s27
	s_cselect_b32 s49, s20, s26
	s_ashr_i32 s17, s16, 31
	s_lshl_b64 s[22:23], s[16:17], 20
	s_add_u32 s22, s34, s22
	s_addc_u32 s23, s35, s23
	s_and_b64 s[30:31], s[4:5], exec
	s_cselect_b32 s17, s23, s29
	s_cselect_b32 s50, s22, s28
	s_add_u32 s26, s26, 0x80080
	s_addc_u32 s27, s27, 0
	s_add_u32 s51, s28, 0x100
	s_addc_u32 s52, s29, 0
	s_mov_b32 s53, -2
	ds_read_b128 v[146:149], v156
	ds_read_b128 v[170:173], v157
	ds_read_b128 v[174:177], v158
	ds_read_b128 v[178:181], v159
	ds_read_b128 v[182:185], v160
	ds_read_b128 v[188:191], v161
	ds_read_b128 v[192:195], v162
	ds_read_b128 v[196:199], v163
	s_add_u32 s28, s26, 0xfff80080
	s_addc_u32 s29, s27, -1
	s_cmp_eq_u32 s53, 28
	s_cselect_b32 s31, s19, s29
	s_cselect_b32 s30, s49, s28
	s_cselect_b32 s29, s17, s52
	s_cselect_b32 s28, s50, s51
	v_lshl_add_u64 v[232:233], s[26:27], 0, v[138:139]
	s_add_i32 m0, s25, 0xc000
	ds_read_b128 v[200:203], v164
	ds_read_b128 v[204:207], v164 offset:1024
	ds_read_b128 v[208:211], v164 offset:2048
	ds_read_b128 v[212:215], v164 offset:3072
	ds_read_b128 v[216:219], v164 offset:4096
	ds_read_b128 v[220:223], v164 offset:5120
	ds_read_b128 v[224:227], v164 offset:6144
	ds_read_b128 v[228:231], v164 offset:7168
	global_load_lds_dwordx4 v[232:233], off
	v_lshl_add_u64 v[232:233], s[26:27], 0, v[140:141]
	s_add_i32 m0, s25, 0xe000
	s_nop 0
	global_load_lds_dwordx4 v[232:233], off
	s_waitcnt vmcnt(8)
	s_waitcnt lgkmcnt(0)
	s_barrier
	s_setprio 1
	s_waitcnt lgkmcnt(0)
	v_mfma_f32_16x16x32_bf16 v[126:129], v[146:149], v[200:203], 0
	v_mfma_f32_16x16x32_bf16 v[122:125], v[174:177], v[200:203], 0
	v_mfma_f32_16x16x32_bf16 v[118:121], v[146:149], v[208:211], 0
	v_mfma_f32_16x16x32_bf16 v[110:113], v[174:177], v[208:211], 0
	v_mfma_f32_16x16x32_bf16 v[102:105], v[146:149], v[216:219], 0
	v_mfma_f32_16x16x32_bf16 v[94:97], v[174:177], v[216:219], 0
	v_mfma_f32_16x16x32_bf16 v[86:89], v[146:149], v[224:227], 0
	v_mfma_f32_16x16x32_bf16 v[78:81], v[174:177], v[224:227], 0
	v_mfma_f32_16x16x32_bf16 v[126:129], v[170:173], v[204:207], v[126:129]
	v_mfma_f32_16x16x32_bf16 v[122:125], v[178:181], v[204:207], v[122:125]
	v_mfma_f32_16x16x32_bf16 v[118:121], v[170:173], v[212:215], v[118:121]
	v_mfma_f32_16x16x32_bf16 v[110:113], v[178:181], v[212:215], v[110:113]
	v_mfma_f32_16x16x32_bf16 v[102:105], v[170:173], v[220:223], v[102:105]
	v_mfma_f32_16x16x32_bf16 v[94:97], v[178:181], v[220:223], v[94:97]
	v_mfma_f32_16x16x32_bf16 v[86:89], v[170:173], v[228:231], v[86:89]
	v_mfma_f32_16x16x32_bf16 v[78:81], v[178:181], v[228:231], v[78:81]
	s_setprio 0
	s_setprio 1
	v_mfma_f32_16x16x32_bf16 v[114:117], v[182:185], v[200:203], 0
	v_mfma_f32_16x16x32_bf16 v[106:109], v[192:195], v[200:203], 0
	v_mfma_f32_16x16x32_bf16 v[98:101], v[182:185], v[208:211], 0
	v_mfma_f32_16x16x32_bf16 v[90:93], v[192:195], v[208:211], 0
	v_mfma_f32_16x16x32_bf16 v[82:85], v[182:185], v[216:219], 0
	v_mfma_f32_16x16x32_bf16 v[74:77], v[192:195], v[216:219], 0
	v_mfma_f32_16x16x32_bf16 v[70:73], v[182:185], v[224:227], 0
	v_mfma_f32_16x16x32_bf16 v[66:69], v[192:195], v[224:227], 0
	v_mfma_f32_16x16x32_bf16 v[114:117], v[188:191], v[204:207], v[114:117]
	v_mfma_f32_16x16x32_bf16 v[106:109], v[196:199], v[204:207], v[106:109]
	v_mfma_f32_16x16x32_bf16 v[98:101], v[188:191], v[212:215], v[98:101]
	v_mfma_f32_16x16x32_bf16 v[90:93], v[196:199], v[212:215], v[90:93]
	v_mfma_f32_16x16x32_bf16 v[82:85], v[188:191], v[220:223], v[82:85]
	v_mfma_f32_16x16x32_bf16 v[74:77], v[196:199], v[220:223], v[74:77]
	v_mfma_f32_16x16x32_bf16 v[70:73], v[188:191], v[228:231], v[70:73]
	v_mfma_f32_16x16x32_bf16 v[66:69], v[196:199], v[228:231], v[66:69]
	s_setprio 0
	s_barrier
	s_add_i32 s54, s46, s36
	v_lshl_add_u64 v[232:233], s[28:29], 0, v[134:135]
	s_mov_b32 m0, s54
	ds_read_b128 v[200:203], v164 offset:16384
	ds_read_b128 v[204:207], v164 offset:17408
	ds_read_b128 v[208:211], v164 offset:18432
	ds_read_b128 v[212:215], v164 offset:19456
	ds_read_b128 v[216:219], v164 offset:20480
	ds_read_b128 v[220:223], v164 offset:21504
	ds_read_b128 v[224:227], v164 offset:22528
	ds_read_b128 v[228:231], v164 offset:23552
	global_load_lds_dwordx4 v[232:233], off
	s_add_i32 m0, s54, 0x2000
	s_add_u32 s54, s28, 0x80000
	v_lshl_add_u64 v[234:235], s[28:29], 0, v[130:131]
	s_addc_u32 s55, s29, 0
	s_add_i32 s57, s47, s36
	global_load_lds_dwordx4 v[234:235], off
	v_lshl_add_u64 v[236:237], s[54:55], 0, v[134:135]
	s_mov_b32 m0, s57
	v_lshl_add_u64 v[238:239], s[30:31], 0, v[132:133]
	global_load_lds_dwordx4 v[236:237], off
	v_lshl_add_u64 v[236:237], s[54:55], 0, v[130:131]
	s_add_i32 m0, s57, 0x2000
	s_nop 0
	global_load_lds_dwordx4 v[236:237], off
	v_lshl_add_u64 v[236:237], s[30:31], 0, v[136:137]
	s_mov_b32 m0, s25
	s_nop 0
	global_load_lds_dwordx4 v[236:237], off
	s_mov_b32 m0, s39
	s_nop 0
	global_load_lds_dwordx4 v[238:239], off
	s_waitcnt vmcnt(8)
	s_waitcnt lgkmcnt(0)
	s_barrier
	s_setprio 1
	s_waitcnt lgkmcnt(0)
	v_mfma_f32_16x16x32_bf16 v[62:65], v[146:149], v[200:203], 0
	v_mfma_f32_16x16x32_bf16 v[58:61], v[174:177], v[200:203], 0
	v_mfma_f32_16x16x32_bf16 v[54:57], v[146:149], v[208:211], 0
	v_mfma_f32_16x16x32_bf16 v[46:49], v[174:177], v[208:211], 0
	v_mfma_f32_16x16x32_bf16 v[38:41], v[146:149], v[216:219], 0
	v_mfma_f32_16x16x32_bf16 v[30:33], v[174:177], v[216:219], 0
	v_mfma_f32_16x16x32_bf16 v[22:25], v[146:149], v[224:227], 0
	v_mfma_f32_16x16x32_bf16 v[14:17], v[174:177], v[224:227], 0
	v_mfma_f32_16x16x32_bf16 v[62:65], v[170:173], v[204:207], v[62:65]
	v_mfma_f32_16x16x32_bf16 v[58:61], v[178:181], v[204:207], v[58:61]
	v_mfma_f32_16x16x32_bf16 v[54:57], v[170:173], v[212:215], v[54:57]
	v_mfma_f32_16x16x32_bf16 v[46:49], v[178:181], v[212:215], v[46:49]
	v_mfma_f32_16x16x32_bf16 v[38:41], v[170:173], v[220:223], v[38:41]
	v_mfma_f32_16x16x32_bf16 v[30:33], v[178:181], v[220:223], v[30:33]
	v_mfma_f32_16x16x32_bf16 v[22:25], v[170:173], v[228:231], v[22:25]
	v_mfma_f32_16x16x32_bf16 v[14:17], v[178:181], v[228:231], v[14:17]
	s_setprio 0
	s_setprio 1
	v_mfma_f32_16x16x32_bf16 v[50:53], v[182:185], v[200:203], 0
	v_mfma_f32_16x16x32_bf16 v[42:45], v[192:195], v[200:203], 0
	v_mfma_f32_16x16x32_bf16 v[34:37], v[182:185], v[208:211], 0
	v_mfma_f32_16x16x32_bf16 v[26:29], v[192:195], v[208:211], 0
	v_mfma_f32_16x16x32_bf16 v[18:21], v[182:185], v[216:219], 0
	v_mfma_f32_16x16x32_bf16 v[10:13], v[192:195], v[216:219], 0
	v_mfma_f32_16x16x32_bf16 v[6:9], v[182:185], v[224:227], 0
	v_mfma_f32_16x16x32_bf16 v[2:5], v[192:195], v[224:227], 0
	v_mfma_f32_16x16x32_bf16 v[50:53], v[188:191], v[204:207], v[50:53]
	v_mfma_f32_16x16x32_bf16 v[42:45], v[196:199], v[204:207], v[42:45]
	v_mfma_f32_16x16x32_bf16 v[34:37], v[188:191], v[212:215], v[34:37]
	v_mfma_f32_16x16x32_bf16 v[26:29], v[196:199], v[212:215], v[26:29]
	v_mfma_f32_16x16x32_bf16 v[18:21], v[188:191], v[220:223], v[18:21]
	v_mfma_f32_16x16x32_bf16 v[10:13], v[196:199], v[220:223], v[10:13]
	v_mfma_f32_16x16x32_bf16 v[6:9], v[188:191], v[228:231], v[6:9]
	v_mfma_f32_16x16x32_bf16 v[2:5], v[196:199], v[228:231], v[2:5]
	s_setprio 0
	s_barrier
	s_add_i32 s54, 0, 0x18000
	v_add_u32_e32 v146, s54, v152
	v_add_u32_e32 v169, s54, v153
	s_add_i32 s55, 0, 0x1c000
	ds_read_b128 v[146:149], v146
	ds_read_b128 v[170:173], v169
	ds_read_b128 v[174:177], v165
	ds_read_b128 v[178:181], v166
	v_add_u32_e32 v169, s55, v152
	v_add_u32_e32 v187, s55, v153
	ds_read_b128 v[182:185], v169
	ds_read_b128 v[188:191], v187
	ds_read_b128 v[192:195], v167
	ds_read_b128 v[196:199], v168
	s_add_u32 s30, s30, 0x80000
	s_addc_u32 s31, s31, 0
	s_mov_b32 m0, s40
	v_lshl_add_u64 v[240:241], s[30:31], 0, v[136:137]
	ds_read_b128 v[200:203], v164 offset:32768
	ds_read_b128 v[204:207], v164 offset:33792
	ds_read_b128 v[208:211], v164 offset:34816
	ds_read_b128 v[212:215], v164 offset:35840
	ds_read_b128 v[216:219], v164 offset:36864
	ds_read_b128 v[220:223], v164 offset:37888
	ds_read_b128 v[224:227], v164 offset:38912
	ds_read_b128 v[228:231], v164 offset:39936
	global_load_lds_dwordx4 v[240:241], off
	v_lshl_add_u64 v[240:241], s[30:31], 0, v[132:133]
	s_mov_b32 m0, s41
	s_nop 0
	global_load_lds_dwordx4 v[240:241], off
	s_waitcnt vmcnt(8)
	s_waitcnt lgkmcnt(0)
	s_barrier
	s_setprio 1
	s_waitcnt lgkmcnt(0)
	v_mfma_f32_16x16x32_bf16 v[126:129], v[146:149], v[200:203], v[126:129]
	v_mfma_f32_16x16x32_bf16 v[122:125], v[174:177], v[200:203], v[122:125]
	v_mfma_f32_16x16x32_bf16 v[118:121], v[146:149], v[208:211], v[118:121]
	v_mfma_f32_16x16x32_bf16 v[110:113], v[174:177], v[208:211], v[110:113]
	v_mfma_f32_16x16x32_bf16 v[102:105], v[146:149], v[216:219], v[102:105]
	v_mfma_f32_16x16x32_bf16 v[94:97], v[174:177], v[216:219], v[94:97]
	v_mfma_f32_16x16x32_bf16 v[86:89], v[146:149], v[224:227], v[86:89]
	v_mfma_f32_16x16x32_bf16 v[78:81], v[174:177], v[224:227], v[78:81]
	v_mfma_f32_16x16x32_bf16 v[126:129], v[170:173], v[204:207], v[126:129]
	v_mfma_f32_16x16x32_bf16 v[122:125], v[178:181], v[204:207], v[122:125]
	v_mfma_f32_16x16x32_bf16 v[118:121], v[170:173], v[212:215], v[118:121]
	v_mfma_f32_16x16x32_bf16 v[110:113], v[178:181], v[212:215], v[110:113]
	v_mfma_f32_16x16x32_bf16 v[102:105], v[170:173], v[220:223], v[102:105]
	v_mfma_f32_16x16x32_bf16 v[94:97], v[178:181], v[220:223], v[94:97]
	v_mfma_f32_16x16x32_bf16 v[86:89], v[170:173], v[228:231], v[86:89]
	v_mfma_f32_16x16x32_bf16 v[78:81], v[178:181], v[228:231], v[78:81]
	s_setprio 0
	s_setprio 1
	v_mfma_f32_16x16x32_bf16 v[114:117], v[182:185], v[200:203], v[114:117]
	v_mfma_f32_16x16x32_bf16 v[106:109], v[192:195], v[200:203], v[106:109]
	v_mfma_f32_16x16x32_bf16 v[98:101], v[182:185], v[208:211], v[98:101]
	v_mfma_f32_16x16x32_bf16 v[90:93], v[192:195], v[208:211], v[90:93]
	v_mfma_f32_16x16x32_bf16 v[82:85], v[182:185], v[216:219], v[82:85]
	v_mfma_f32_16x16x32_bf16 v[74:77], v[192:195], v[216:219], v[74:77]
	v_mfma_f32_16x16x32_bf16 v[70:73], v[182:185], v[224:227], v[70:73]
	v_mfma_f32_16x16x32_bf16 v[66:69], v[192:195], v[224:227], v[66:69]
	v_mfma_f32_16x16x32_bf16 v[114:117], v[188:191], v[204:207], v[114:117]
	v_mfma_f32_16x16x32_bf16 v[106:109], v[196:199], v[204:207], v[106:109]
	v_mfma_f32_16x16x32_bf16 v[98:101], v[188:191], v[212:215], v[98:101]
	v_mfma_f32_16x16x32_bf16 v[90:93], v[196:199], v[212:215], v[90:93]
	v_mfma_f32_16x16x32_bf16 v[82:85], v[188:191], v[220:223], v[82:85]
	v_mfma_f32_16x16x32_bf16 v[74:77], v[196:199], v[220:223], v[74:77]
	v_mfma_f32_16x16x32_bf16 v[70:73], v[188:191], v[228:231], v[70:73]
	v_mfma_f32_16x16x32_bf16 v[66:69], v[196:199], v[228:231], v[66:69]
	s_setprio 0
	s_barrier
	s_add_i32 s30, s54, s36
	v_lshl_add_u64 v[232:233], v[232:233], 0, s[12:13]
	s_mov_b32 m0, s30
	ds_read_b128 v[200:203], v164 offset:49152
	ds_read_b128 v[204:207], v164 offset:50176
	ds_read_b128 v[208:211], v164 offset:51200
	ds_read_b128 v[212:215], v164 offset:52224
	ds_read_b128 v[216:219], v164 offset:53248
	ds_read_b128 v[220:223], v164 offset:54272
	ds_read_b128 v[224:227], v164 offset:55296
	ds_read_b128 v[228:231], v164 offset:56320
	global_load_lds_dwordx4 v[232:233], off
	s_add_i32 m0, s30, 0x2000
	s_add_u32 s28, s28, 0x80080
	v_lshl_add_u64 v[232:233], v[234:235], 0, s[12:13]
	s_addc_u32 s29, s29, 0
	s_add_i32 s30, s55, s36
	global_load_lds_dwordx4 v[232:233], off
	v_lshl_add_u64 v[232:233], s[28:29], 0, v[134:135]
	s_mov_b32 m0, s30
	s_nop 0
	global_load_lds_dwordx4 v[232:233], off
	v_lshl_add_u64 v[232:233], s[28:29], 0, v[130:131]
	s_add_i32 m0, s30, 0x2000
	s_nop 0
	global_load_lds_dwordx4 v[232:233], off
	v_lshl_add_u64 v[232:233], v[236:237], 0, s[12:13]
	s_mov_b32 m0, s43
	s_nop 0
	global_load_lds_dwordx4 v[232:233], off
	v_lshl_add_u64 v[232:233], v[238:239], 0, s[12:13]
	s_mov_b32 m0, s44
	s_nop 0
	global_load_lds_dwordx4 v[232:233], off
	s_waitcnt vmcnt(8)
	s_waitcnt lgkmcnt(0)
	s_barrier
	s_setprio 1
	s_waitcnt lgkmcnt(0)
	v_mfma_f32_16x16x32_bf16 v[62:65], v[146:149], v[200:203], v[62:65]
	v_mfma_f32_16x16x32_bf16 v[58:61], v[174:177], v[200:203], v[58:61]
	v_mfma_f32_16x16x32_bf16 v[54:57], v[146:149], v[208:211], v[54:57]
	v_mfma_f32_16x16x32_bf16 v[46:49], v[174:177], v[208:211], v[46:49]
	v_mfma_f32_16x16x32_bf16 v[38:41], v[146:149], v[216:219], v[38:41]
	v_mfma_f32_16x16x32_bf16 v[30:33], v[174:177], v[216:219], v[30:33]
	v_mfma_f32_16x16x32_bf16 v[22:25], v[146:149], v[224:227], v[22:25]
	v_mfma_f32_16x16x32_bf16 v[14:17], v[174:177], v[224:227], v[14:17]
	v_mfma_f32_16x16x32_bf16 v[62:65], v[170:173], v[204:207], v[62:65]
	v_mfma_f32_16x16x32_bf16 v[58:61], v[178:181], v[204:207], v[58:61]
	v_mfma_f32_16x16x32_bf16 v[54:57], v[170:173], v[212:215], v[54:57]
	v_mfma_f32_16x16x32_bf16 v[46:49], v[178:181], v[212:215], v[46:49]
	v_mfma_f32_16x16x32_bf16 v[38:41], v[170:173], v[220:223], v[38:41]
	v_mfma_f32_16x16x32_bf16 v[30:33], v[178:181], v[220:223], v[30:33]
	v_mfma_f32_16x16x32_bf16 v[22:25], v[170:173], v[228:231], v[22:25]
	v_mfma_f32_16x16x32_bf16 v[14:17], v[178:181], v[228:231], v[14:17]
	s_setprio 0
	s_setprio 1
	v_mfma_f32_16x16x32_bf16 v[50:53], v[182:185], v[200:203], v[50:53]
	v_mfma_f32_16x16x32_bf16 v[42:45], v[192:195], v[200:203], v[42:45]
	v_mfma_f32_16x16x32_bf16 v[34:37], v[182:185], v[208:211], v[34:37]
	v_mfma_f32_16x16x32_bf16 v[26:29], v[192:195], v[208:211], v[26:29]
	v_mfma_f32_16x16x32_bf16 v[18:21], v[182:185], v[216:219], v[18:21]
	v_mfma_f32_16x16x32_bf16 v[10:13], v[192:195], v[216:219], v[10:13]
	v_mfma_f32_16x16x32_bf16 v[6:9], v[182:185], v[224:227], v[6:9]
	v_mfma_f32_16x16x32_bf16 v[2:5], v[192:195], v[224:227], v[2:5]
	v_mfma_f32_16x16x32_bf16 v[50:53], v[188:191], v[204:207], v[50:53]
	v_mfma_f32_16x16x32_bf16 v[42:45], v[196:199], v[204:207], v[42:45]
	v_mfma_f32_16x16x32_bf16 v[34:37], v[188:191], v[212:215], v[34:37]
	v_mfma_f32_16x16x32_bf16 v[26:29], v[196:199], v[212:215], v[26:29]
	v_mfma_f32_16x16x32_bf16 v[18:21], v[188:191], v[220:223], v[18:21]
	v_mfma_f32_16x16x32_bf16 v[10:13], v[196:199], v[220:223], v[10:13]
	v_mfma_f32_16x16x32_bf16 v[6:9], v[188:191], v[228:231], v[6:9]
	v_mfma_f32_16x16x32_bf16 v[2:5], v[196:199], v[228:231], v[2:5]
	s_setprio 0
	s_barrier
	s_add_i32 s53, s53, 2
	s_add_u32 s26, s26, 0x100
	s_addc_u32 s27, s27, 0
	s_add_u32 s51, s51, 0x100
	s_addc_u32 s52, s52, 0
